# attention phases: one static s_setprio 1 for waves 0-3 instead (other half)
# speedup vs baseline: 1.0073x; 1.0041x over previous
; __device__ __forceinline__ void phase_pool(const Frame& F, bool dry) {
;     const bf16_t* UB = (const bf16_t*)(F.ws + AR_UB); bf16_t* PB = (bf16_t*)(F.ws + AR_PB);
;     const int gw = F.bid * NWAVES + F.wave, NGW = F.G * NWAVES, lane = F.lane;
;     for (int it = gw; it < 4 * (NTOK / 64); it += NGW) { const int g = it & 3, it4 = it >> 2; const int strip = 4 * it4 + (lane >> 4), ch = 16 * g + (lane & 15), t0 = strip * 16;
.LBB0_506:
	s_or_b64 exec, exec, s[0:1]
	s_xor_b64 s[0:1], s[34:35], -1
	v_writelane_b32 v255, s0, 24
	s_waitcnt lgkmcnt(0)
	s_barrier
	v_writelane_b32 v255, s1, 25
	v_readlane_b32 s0, v254, 17
	s_nop 1
	s_cmpk_le_i32 s0, 0xff00
	s_cbranch_scc1 .Lprio_a2
	s_setprio 1

; #define OPAQUE_WS() unsigned char* ws = P.ws; asm volatile("" : "+s"(ws)); F.ws = ws; F.tid = fresh_tid(F.wave); asm volatile("" : "+v"(F.tid)); F.lane = F.tid & 63; int c = F.bid; asm volatile("" : "+s"(c))
; #define REP_BEGIN(k) for (int rep_ = 0, nrep_ = ((k) >= PROBE_LO && (k) < PROBE_HI) ? PROBE_N : 0; rep_ <= nrep_; ++rep_) { const bool rerun = PROBE_AFTER ? (rep_ > 0) : (rep_ < nrep_), dry = rerun && PROBE_DRY_;
; __global__ void __launch_bounds__(NTHREADS, 2) mk_fwd(Params P) {
;     ...
;         if (PH_EN(5) && IN(pb + 5)) { REP_BEGIN(pb + 5) OPAQUE_WS(); int lq = l; asm volatile("" : "+s"(lq));
;     ...
;             att::XArgs A{(const bf16_t*)(ws + AR_QX), (const bf16_t*)(ws + WS_KXV) + (size_t)lq * B * MEM * 1024, (bf16_t*)(ws + AR_OX), P.in[20] + lq * XHD, dry};
;             for (int u = c, rnd = 0; u < B * XH * (S / 256); u += G, ++rnd) { int qt = u & 15, h = (u >> 4) & 3, b = u >> 6;
;                 if (G == 256) { const int idx = rnd * 32 + (c >> 3), bh = (c & 7) * 4 + (idx >> 4); qt = idx & 15; h = bh & 3; b = bh >> 2; }
;                 att::xattn_unit(A, b, h, qt, F.lds, F.wave); }
.LBB0_1221:
	s_or_b64 exec, exec, s[0:1]
	v_readlane_b32 s2, v253, 1
	v_readlane_b32 s3, v253, 2
	s_mov_b32 s0, s93
	s_waitcnt lgkmcnt(0)
	s_barrier
	v_readlane_b32 s18, v254, 17
	s_nop 1
	s_cmpk_le_i32 s18, 0xff00
	s_cbranch_scc1 .Lprio_x2
	s_setprio 1
